# P6/P10 LayerNorm wave sums: DPP row ops + permlane16/32 swap all-reduce instead of six serial ds_bpermute round trips (pure chains only)
# speedup vs baseline: 1.0059x; 1.0029x over previous
.LBB0_986:
	v_mov_b32_e32 v246, v191
	v_mov_b32_e32 v247, v192
	v_mov_b32_e32 v248, v190
	v_mov_b32_e32 v249, v193
	v_pk_add_f32 v[246:247], v[246:247], v[248:249]
	v_mov_b32_e32 v248, v187
	v_mov_b32_e32 v249, v188
	v_mov_b32_e32 v216, v186
	v_mov_b32_e32 v217, v189
	v_pk_add_f32 v[216:217], v[248:249], v[216:217]
	v_add_f32_e32 v209, v246, v247
	v_pk_add_f32 v[216:217], v[216:217], v[216:217] op_sel:[0,1] op_sel_hi:[1,0]
	v_add_f32_e32 v246, 0, v209
	v_add_f32_e32 v248, v182, v183
	v_add_f32_e32 v218, v184, v185
	v_mov_b32_e32 v247, v178
	v_mov_b32_e32 v217, v179
	v_mov_b32_e32 v249, v180
	v_mov_b32_e32 v219, v181
	v_pk_add_f32 v[216:217], v[246:247], v[216:217]
	v_pk_add_f32 v[218:219], v[248:249], v[218:219]
	s_mov_b32 s36, 0xf800000
	v_pk_add_f32 v[216:217], v[216:217], v[218:219]
	s_nop 0
	v_add_f32_e32 v209, v216, v217
	s_nop 1
	v_add_f32_dpp v209, v209, v209 quad_perm:[1,0,3,2] row_mask:0xf bank_mask:0xf
	s_nop 1
	v_add_f32_dpp v209, v209, v209 quad_perm:[2,3,0,1] row_mask:0xf bank_mask:0xf
	s_nop 1
	v_add_f32_dpp v209, v209, v209 row_half_mirror row_mask:0xf bank_mask:0xf
	s_nop 1
	v_add_f32_dpp v209, v209, v209 row_mirror row_mask:0xf bank_mask:0xf
	v_mov_b32_e32 v216, v209
	s_nop 1
	v_permlane16_swap_b32_e32 v216, v209
	s_nop 1
	v_add_f32_e32 v209, v209, v216
	v_mov_b32_e32 v216, v209
	s_nop 1
	v_permlane32_swap_b32_e32 v216, v209
	s_nop 1
	v_add_f32_e32 v209, v209, v216
	v_fmamk_f32 v191, v209, 0xba800000, v191
	v_fmamk_f32 v190, v209, 0xba800000, v190
	v_fmamk_f32 v193, v209, 0xba800000, v193
	v_fmac_f32_e32 v192, 0xba800000, v209
	v_pk_mul_f32 v[216:217], v[192:193], v[192:193]
	v_pk_mul_f32 v[218:219], v[190:191], v[190:191]
	v_fmamk_f32 v187, v209, 0xba800000, v187
	v_fmamk_f32 v186, v209, 0xba800000, v186
	v_fmamk_f32 v189, v209, 0xba800000, v189
	v_pk_mov_b32 v[246:247], v[218:219], v[216:217] op_sel:[1,0]
	v_mov_b32_e32 v219, v217
	v_fmac_f32_e32 v188, 0xba800000, v209
	v_pk_add_f32 v[216:217], v[246:247], v[218:219]
	v_pk_mul_f32 v[218:219], v[188:189], v[188:189]
	v_pk_mul_f32 v[246:247], v[186:187], v[186:187]
	v_fmac_f32_e32 v184, 0xba800000, v209
	v_pk_mov_b32 v[248:249], v[246:247], v[218:219] op_sel:[1,0]
	v_mov_b32_e32 v247, v219
	v_pk_add_f32 v[218:219], v[248:249], v[246:247]
	v_fmamk_f32 v246, v209, 0xba800000, v182
	v_fmamk_f32 v247, v209, 0xba800000, v183
	v_mul_f32_e32 v182, v246, v246
	v_pk_fma_f32 v[182:183], v[246:247], v[246:247], v[182:183] op_sel_hi:[1,1,0]
	v_fmamk_f32 v185, v209, 0xba800000, v185
	v_mul_f32_e32 v182, v184, v184
	v_pk_add_f32 v[216:217], v[216:217], v[216:217] op_sel_hi:[0,1]
	v_pk_add_f32 v[218:219], v[218:219], v[218:219] op_sel_hi:[0,1]
	v_pk_fma_f32 v[248:249], v[184:185], v[184:185], v[182:183] op_sel_hi:[1,1,0]
	v_fmamk_f32 v181, v209, 0xba800000, v181
	v_fmamk_f32 v180, v209, 0xba800000, v180
	v_fmamk_f32 v179, v209, 0xba800000, v179
	v_fmac_f32_e32 v178, 0xba800000, v209
	v_mul_f32_e32 v182, v178, v178
	v_mul_f32_e32 v248, v179, v179
	v_mul_f32_e32 v216, v180, v180
	v_mul_f32_e32 v218, v181, v181
	v_pk_add_f32 v[182:183], v[182:183], v[248:249]
	v_pk_add_f32 v[216:217], v[216:217], v[218:219]
	s_nop 0
	v_pk_add_f32 v[182:183], v[182:183], v[216:217]
	s_nop 0
	v_add_f32_e32 v182, v182, v183
	s_nop 1
	v_add_f32_dpp v182, v182, v182 quad_perm:[1,0,3,2] row_mask:0xf bank_mask:0xf
	s_nop 1
	v_add_f32_dpp v182, v182, v182 quad_perm:[2,3,0,1] row_mask:0xf bank_mask:0xf
	s_nop 1
	v_add_f32_dpp v182, v182, v182 row_half_mirror row_mask:0xf bank_mask:0xf
	s_nop 1
	v_add_f32_dpp v182, v182, v182 row_mirror row_mask:0xf bank_mask:0xf
	v_mov_b32_e32 v183, v182
	s_nop 1
	v_permlane16_swap_b32_e32 v183, v182
	s_nop 1
	v_add_f32_e32 v182, v182, v183
	v_mov_b32_e32 v183, v182
	s_nop 1
	v_permlane32_swap_b32_e32 v183, v182
	s_nop 1
	v_add_f32_e32 v182, v182, v183
	v_fmamk_f32 v182, v182, 0x3a800000, v211
	v_mul_f32_e32 v183, 0x4f800000, v182
	v_cmp_gt_f32_e32 vcc, s36, v182
	s_nop 1
	v_cndmask_b32_e32 v182, v182, v183, vcc
	v_sqrt_f32_e32 v183, v182
	s_nop 0
	v_add_u32_e32 v209, -1, v183
	v_add_u32_e32 v216, 1, v183
	v_fma_f32 v217, -v209, v183, v182
	v_fma_f32 v218, -v216, v183, v182
	v_cmp_ge_f32_e64 s[12:13], 0, v217
	s_nop 1
	v_cndmask_b32_e64 v183, v183, v209, s[12:13]
	v_cmp_lt_f32_e64 s[12:13], 0, v218
	s_nop 1
	v_cndmask_b32_e64 v183, v183, v216, s[12:13]
	v_mul_f32_e32 v209, 0x37800000, v183
	v_cndmask_b32_e32 v183, v183, v209, vcc
	v_cmp_class_f32_e32 vcc, v182, v212
	s_nop 1
	v_cndmask_b32_e32 v182, v183, v182, vcc
	v_div_scale_f32 v183, s[12:13], v182, v182, 1.0
	v_rcp_f32_e32 v209, v183
	v_readlane_b32 s12, v252, 4
	s_add_i32 s34, s12, s14
	s_ashr_i32 s35, s34, 31
	v_fma_f32 v216, -v183, v209, 1.0
	v_fmac_f32_e32 v209, v216, v209
	v_div_scale_f32 v216, vcc, 1.0, v182, 1.0
	v_mul_f32_e32 v217, v216, v209
	v_fma_f32 v218, -v183, v217, v216
	v_fmac_f32_e32 v217, v218, v209
	v_fma_f32 v183, -v183, v217, v216
	v_div_fmas_f32 v183, v183, v209, v217
	v_div_fixup_f32 v182, v183, v182, 1.0
	v_pk_mul_f32 v[190:191], v[190:191], v[182:183] op_sel_hi:[1,0]
	s_lshl_b64 s[12:13], s[34:35], 10
	s_waitcnt vmcnt(22)
	v_pk_fma_f32 v[190:191], v[2:3], v[190:191], v[6:7]
	v_pk_mul_f32 v[192:193], v[192:193], v[182:183] op_sel_hi:[1,0]
	v_pk_fma_f32 v[190:191], v[98:99], v[190:191], v[118:119]
	s_mov_b32 s35, 0xffff
	v_cvt_pk_bf16_f32 v216, v191, 0
	v_cvt_pk_bf16_f32 v183, v190, 0
	v_lshlrev_b32_e32 v216, 16, v216
	v_lshlrev_b32_e32 v209, 16, v183
	v_sub_f32_e32 v217, v191, v216
	v_and_or_b32 v216, v183, s35, v216
	v_mov_b32_e32 v183, v1
	v_cvt_pk_fp8_f32 v183, v190, v191
	v_pk_fma_f32 v[192:193], v[4:5], v[192:193], v[8:9]
	v_cvt_pk_bf16_f32 v218, v217, 0
	v_pk_fma_f32 v[192:193], v[100:101], v[192:193], v[120:121]
	v_sub_f32_e32 v209, v190, v209
	v_cvt_pk_fp8_f32 v183, v192, v193 op_sel:[0,0,1]
	v_cvt_pk_bf16_f32 v217, v192, 0
	v_cvt_pk_bf16_f32 v248, v193, 0
	v_lshlrev_b32_e32 v219, 16, v217
	v_lshlrev_b32_e32 v248, 16, v248
	v_sub_f32_e32 v219, v192, v219
	v_sub_f32_e32 v249, v193, v248
	v_lshl_add_u64 v[192:193], v[202:203], 0, s[12:13]
	global_store_dword v[192:193], v183, off
	v_add_u32_e32 v183, s47, v234
	v_pk_mul_f32 v[186:187], v[186:187], v[182:183] op_sel_hi:[1,0]
	v_cvt_pk_bf16_f32 v249, v249, 0
	s_waitcnt vmcnt(20)
	v_pk_fma_f32 v[186:187], v[10:11], v[186:187], v[18:19]
	v_cvt_pk_bf16_f32 v209, v209, 0
	v_cvt_pk_bf16_f32 v219, v219, 0
	v_and_or_b32 v217, v217, s35, v248
	v_lshlrev_b32_e32 v190, 16, v218
	v_lshlrev_b32_e32 v191, 16, v249
	v_pk_fma_f32 v[186:187], v[138:139], v[186:187], v[142:143]
	v_and_or_b32 v190, v209, s35, v190
	v_and_or_b32 v191, v219, s35, v191
	ds_write_b64 v183, v[216:217]
	ds_write_b64 v183, v[190:191] offset:33024
	v_pk_mul_f32 v[188:189], v[188:189], v[182:183] op_sel_hi:[1,0]
	v_cvt_pk_bf16_f32 v183, v186, 0
	v_lshlrev_b32_e32 v190, 16, v183
	v_sub_f32_e32 v190, v186, v190
	v_cvt_pk_bf16_f32 v192, v190, 0
	v_cvt_pk_bf16_f32 v190, v187, 0
	v_lshlrev_b32_e32 v190, 16, v190
	v_sub_f32_e32 v191, v187, v190
	v_cvt_pk_bf16_f32 v193, v191, 0
	v_and_or_b32 v190, v183, s35, v190
	v_lshlrev_b32_e32 v183, 16, v193
	v_mov_b32_e32 v193, v1
	v_pk_fma_f32 v[188:189], v[12:13], v[188:189], v[20:21]
	v_cvt_pk_fp8_f32 v193, v186, v187
	v_pk_fma_f32 v[188:189], v[140:141], v[188:189], v[144:145]
	s_add_u32 s12, s20, s12
	v_cvt_pk_bf16_f32 v216, v189, 0
	v_cvt_pk_bf16_f32 v191, v188, 0
	v_lshlrev_b32_e32 v216, 16, v216
	v_lshlrev_b32_e32 v209, 16, v191
	v_sub_f32_e32 v217, v189, v216
	v_cvt_pk_fp8_f32 v193, v188, v189 op_sel:[0,0,1]
	v_sub_f32_e32 v209, v188, v209
	v_cvt_pk_bf16_f32 v217, v217, 0
	v_cvt_pk_bf16_f32 v209, v209, 0
	v_and_or_b32 v186, v192, s35, v183
	v_lshlrev_b32_e32 v183, 16, v217
	s_addc_u32 s13, s21, s13
	v_and_or_b32 v191, v191, s35, v216
	v_and_or_b32 v187, v209, s35, v183
	v_lshl_add_u64 v[188:189], s[12:13], 0, v[0:1]
	v_add_u32_e32 v183, s47, v235
	global_store_dword v[188:189], v193, off
	ds_write_b64 v183, v[190:191]
	ds_write_b64 v183, v[186:187] offset:33024
	v_pk_mul_f32 v[186:187], v[246:247], v[182:183] op_sel_hi:[1,0]
	v_pk_mul_f32 v[184:185], v[184:185], v[182:183] op_sel_hi:[1,0]
	s_waitcnt vmcnt(20)
	v_pk_fma_f32 v[186:187], v[14:15], v[186:187], v[22:23]
	v_pk_fma_f32 v[184:185], v[16:17], v[184:185], v[24:25]
	v_pk_fma_f32 v[186:187], v[150:151], v[186:187], v[146:147]
	v_pk_fma_f32 v[184:185], v[152:153], v[184:185], v[148:149]
	v_cvt_pk_bf16_f32 v183, v186, 0
	v_lshlrev_b32_e32 v188, 16, v183
	v_sub_f32_e32 v188, v186, v188
	v_cvt_pk_bf16_f32 v209, v188, 0
	v_cvt_pk_bf16_f32 v188, v187, 0
	v_lshlrev_b32_e32 v218, 16, v188
	v_sub_f32_e32 v188, v187, v218
	v_cvt_pk_bf16_f32 v246, v184, 0
	v_cvt_pk_bf16_f32 v219, v188, 0
	v_lshlrev_b32_e32 v188, 16, v246
	v_sub_f32_e32 v188, v184, v188
	v_cvt_pk_bf16_f32 v247, v188, 0
	v_mov_b32_e32 v188, v175
	v_mov_b32_e32 v189, v176
	v_mov_b32_e32 v190, v174
	v_mov_b32_e32 v191, v177
	v_pk_add_f32 v[188:189], v[188:189], v[190:191]
	v_mov_b32_e32 v190, v171
	v_mov_b32_e32 v191, v172
	v_mov_b32_e32 v192, v170
	v_mov_b32_e32 v193, v173
	v_pk_add_f32 v[190:191], v[190:191], v[192:193]
	v_add_f32_e32 v188, v188, v189
	v_pk_add_f32 v[190:191], v[190:191], v[190:191] op_sel:[0,1] op_sel_hi:[1,0]
	v_add_f32_e32 v188, 0, v188
	v_add_f32_e32 v192, v166, v167
	v_add_f32_e32 v216, v168, v169
	v_mov_b32_e32 v189, v162
	v_mov_b32_e32 v191, v163
	v_mov_b32_e32 v193, v164
	v_mov_b32_e32 v217, v165
	v_pk_add_f32 v[188:189], v[188:189], v[190:191]
	v_pk_add_f32 v[190:191], v[192:193], v[216:217]
	v_cvt_pk_bf16_f32 v248, v185, 0
	v_pk_add_f32 v[188:189], v[188:189], v[190:191]
	v_lshlrev_b32_e32 v191, 16, v248
	v_add_f32_e32 v189, v188, v189
	ds_bpermute_b32 v190, v226, v189
	v_sub_f32_e32 v188, v185, v191
	v_cvt_pk_bf16_f32 v192, v188, 0
	v_and_or_b32 v188, v183, s35, v218
	v_mov_b32_e32 v193, v1
	s_waitcnt lgkmcnt(0)
	v_add_f32_e32 v183, v189, v190
	ds_bpermute_b32 v190, v227, v183
	v_cvt_pk_fp8_f32 v193, v186, v187
	v_and_or_b32 v189, v246, s35, v191
	v_lshlrev_b32_e32 v191, 16, v219
	v_and_or_b32 v186, v209, s35, v191
	s_waitcnt lgkmcnt(0)
	v_add_f32_e32 v183, v183, v190
	ds_bpermute_b32 v190, v228, v183
	v_cvt_pk_fp8_f32 v193, v184, v185 op_sel:[0,0,1]
	v_lshl_add_u64 v[184:185], s[12:13], 0, v[198:199]
	v_lshlrev_b32_e32 v187, 16, v192
	v_and_or_b32 v187, v247, s35, v187
	s_waitcnt lgkmcnt(0)
	v_add_f32_e32 v183, v183, v190
	ds_bpermute_b32 v190, v229, v183
	global_store_dword v[184:185], v193, off
	v_add_u32_e32 v184, s47, v236
	ds_write_b64 v184, v[188:189]
	ds_write_b64 v184, v[186:187] offset:33024
	s_waitcnt lgkmcnt(2)
	v_add_f32_e32 v183, v183, v190
	ds_bpermute_b32 v185, v230, v183
	v_pk_mul_f32 v[180:181], v[180:181], v[182:183] op_sel_hi:[1,0]
	v_pk_mul_f32 v[178:179], v[178:179], v[182:183] op_sel_hi:[1,0]
	s_waitcnt vmcnt(19)
	v_pk_fma_f32 v[180:181], v[28:29], v[180:181], v[32:33]
	v_pk_fma_f32 v[178:179], v[26:27], v[178:179], v[30:31]
	s_waitcnt lgkmcnt(0)
	v_add_f32_e32 v182, v183, v185
	ds_bpermute_b32 v183, v231, v182
	s_waitcnt vmcnt(3)
	v_pk_fma_f32 v[180:181], v[156:157], v[180:181], v[160:161]
	v_pk_fma_f32 v[178:179], v[154:155], v[178:179], v[158:159]
	s_waitcnt lgkmcnt(0)
	v_add_f32_e32 v191, v182, v183
	v_fmamk_f32 v175, v191, 0xba800000, v175
	v_fmamk_f32 v174, v191, 0xba800000, v174
	v_fmamk_f32 v177, v191, 0xba800000, v177
	v_fmac_f32_e32 v176, 0xba800000, v191
	v_pk_mul_f32 v[182:183], v[176:177], v[176:177]
	v_pk_mul_f32 v[184:185], v[174:175], v[174:175]
	v_fmamk_f32 v171, v191, 0xba800000, v171
	v_pk_mov_b32 v[186:187], v[184:185], v[182:183] op_sel:[1,0]
	v_mov_b32_e32 v185, v183
	v_pk_add_f32 v[182:183], v[186:187], v[184:185]
	v_fmamk_f32 v170, v191, 0xba800000, v170
	v_fmamk_f32 v173, v191, 0xba800000, v173
	v_fmac_f32_e32 v172, 0xba800000, v191
	v_pk_add_f32 v[182:183], v[182:183], v[182:183] op_sel_hi:[0,1]
	v_pk_mul_f32 v[184:185], v[172:173], v[172:173]
	v_pk_mul_f32 v[186:187], v[170:171], v[170:171]
	v_fmamk_f32 v166, v191, 0xba800000, v166
	v_pk_mov_b32 v[188:189], v[186:187], v[184:185] op_sel:[1,0]
	v_mov_b32_e32 v187, v185
	v_fmamk_f32 v167, v191, 0xba800000, v167
	v_fmac_f32_e32 v168, 0xba800000, v191
	v_mul_f32_e32 v182, v166, v166
	v_pk_add_f32 v[184:185], v[188:189], v[186:187]
	v_fmamk_f32 v169, v191, 0xba800000, v169
	v_pk_fma_f32 v[186:187], v[166:167], v[166:167], v[182:183] op_sel_hi:[1,1,0]
	v_mul_f32_e32 v182, v168, v168
	v_pk_add_f32 v[184:185], v[184:185], v[184:185] op_sel_hi:[0,1]
	v_pk_fma_f32 v[188:189], v[168:169], v[168:169], v[182:183] op_sel_hi:[1,1,0]
	v_fmamk_f32 v165, v191, 0xba800000, v165
	v_fmamk_f32 v164, v191, 0xba800000, v164
	v_fmamk_f32 v163, v191, 0xba800000, v163
	v_fmac_f32_e32 v162, 0xba800000, v191
	v_mul_f32_e32 v186, v162, v162
	v_mul_f32_e32 v188, v163, v163
	v_mul_f32_e32 v182, v164, v164
	v_mul_f32_e32 v184, v165, v165
	v_pk_add_f32 v[186:187], v[186:187], v[188:189]
	v_pk_add_f32 v[182:183], v[182:183], v[184:185]
	v_cvt_pk_bf16_f32 v189, v181, 0
	v_pk_add_f32 v[182:183], v[186:187], v[182:183]
	v_cvt_pk_bf16_f32 v185, v179, 0
	v_add_f32_e32 v182, v182, v183
	ds_bpermute_b32 v183, v226, v182
	v_lshlrev_b32_e32 v189, 16, v189
	v_cvt_pk_bf16_f32 v190, v178, 0
	v_lshlrev_b32_e32 v185, 16, v185
	v_sub_f32_e32 v186, v179, v185
	s_waitcnt lgkmcnt(0)
	v_add_f32_e32 v182, v182, v183
	ds_bpermute_b32 v183, v227, v182
	v_lshlrev_b32_e32 v184, 16, v190
	v_cvt_pk_bf16_f32 v187, v180, 0
	v_lshlrev_b32_e32 v188, 16, v187
	v_sub_f32_e32 v188, v180, v188
	s_waitcnt lgkmcnt(0)
	v_add_f32_e32 v182, v182, v183
	ds_bpermute_b32 v183, v228, v182
	v_sub_f32_e32 v184, v178, v184
	v_cvt_pk_bf16_f32 v186, v186, 0
	v_cvt_pk_bf16_f32 v184, v184, 0
	v_lshlrev_b32_e32 v186, 16, v186
	s_waitcnt lgkmcnt(0)
	v_add_f32_e32 v183, v182, v183
	ds_bpermute_b32 v191, v229, v183
	v_sub_f32_e32 v182, v181, v189
	v_cvt_pk_bf16_f32 v192, v182, 0
	v_and_or_b32 v182, v190, s35, v185
	v_cvt_pk_bf16_f32 v188, v188, 0
	s_waitcnt lgkmcnt(0)
	v_add_f32_e32 v185, v183, v191
	ds_bpermute_b32 v190, v230, v185
	v_and_or_b32 v183, v187, s35, v189
	v_mov_b32_e32 v187, v1
	v_cvt_pk_fp8_f32 v187, v178, v179
	v_and_or_b32 v178, v184, s35, v186
	s_waitcnt lgkmcnt(0)
	v_add_f32_e32 v185, v185, v190
	ds_bpermute_b32 v189, v231, v185
	v_cvt_pk_fp8_f32 v187, v180, v181 op_sel:[0,0,1]
	v_lshlrev_b32_e32 v179, 16, v192
	v_and_or_b32 v179, v188, s35, v179
	s_waitcnt lgkmcnt(0)
	v_add_f32_e32 v180, v185, v189
	v_fmamk_f32 v180, v180, 0x3a800000, v211
	v_mul_f32_e32 v181, 0x4f800000, v180
	v_cmp_gt_f32_e32 vcc, s36, v180
	s_nop 1
	v_cndmask_b32_e32 v184, v180, v181, vcc
	v_sqrt_f32_e32 v185, v184
	v_lshl_add_u64 v[180:181], s[12:13], 0, v[200:201]
	global_store_dword v[180:181], v187, off
	v_add_u32_e32 v180, s47, v237
	v_add_u32_e32 v181, -1, v185
	v_fma_f32 v186, -v181, v185, v184
	v_cmp_ge_f32_e64 s[12:13], 0, v186
	v_add_u32_e32 v186, 1, v185
	ds_write_b64 v180, v[182:183]
	ds_write_b64 v180, v[178:179] offset:33024
	v_cndmask_b32_e64 v181, v185, v181, s[12:13]
	v_fma_f32 v185, -v186, v185, v184
	v_cmp_lt_f32_e64 s[12:13], 0, v185
	s_nop 1
	v_cndmask_b32_e64 v181, v181, v186, s[12:13]
	v_mul_f32_e32 v185, 0x37800000, v181
	v_cndmask_b32_e32 v181, v181, v185, vcc
	v_cmp_class_f32_e32 vcc, v184, v212
	s_nop 1
	v_cndmask_b32_e32 v181, v181, v184, vcc
	v_div_scale_f32 v184, s[12:13], v181, v181, 1.0
	v_rcp_f32_e32 v185, v184
	s_add_i32 s12, s34, 1
	s_ashr_i32 s13, s12, 31
	s_lshl_b64 s[12:13], s[12:13], 10
	v_fma_f32 v178, -v184, v185, 1.0
	v_fmac_f32_e32 v185, v178, v185
	v_div_scale_f32 v178, vcc, 1.0, v181, 1.0
	v_mul_f32_e32 v179, v178, v185
	v_fma_f32 v180, -v184, v179, v178
	v_fmac_f32_e32 v179, v180, v185
	v_fma_f32 v178, -v184, v179, v178
	v_div_fmas_f32 v178, v178, v185, v179
	v_div_fixup_f32 v178, v178, v181, 1.0
	v_pk_mul_f32 v[174:175], v[174:175], v[178:179] op_sel_hi:[1,0]
	v_pk_mul_f32 v[176:177], v[176:177], v[178:179] op_sel_hi:[1,0]
	v_pk_fma_f32 v[174:175], v[2:3], v[174:175], v[6:7]
	v_pk_fma_f32 v[176:177], v[4:5], v[176:177], v[8:9]
	v_pk_fma_f32 v[174:175], v[98:99], v[174:175], v[118:119]
	v_pk_fma_f32 v[176:177], v[100:101], v[176:177], v[120:121]
	v_cvt_pk_bf16_f32 v179, v174, 0
	v_lshlrev_b32_e32 v180, 16, v179
	v_sub_f32_e32 v180, v174, v180
	v_cvt_pk_bf16_f32 v182, v180, 0
	v_cvt_pk_bf16_f32 v180, v175, 0
	v_lshlrev_b32_e32 v180, 16, v180
	v_sub_f32_e32 v181, v175, v180
	v_and_or_b32 v180, v179, s35, v180
	v_mov_b32_e32 v179, v1
	v_cvt_pk_fp8_f32 v179, v174, v175
	v_cvt_pk_bf16_f32 v185, v177, 0
	v_cvt_pk_bf16_f32 v183, v181, 0
	v_cvt_pk_bf16_f32 v181, v176, 0
	v_cvt_pk_fp8_f32 v179, v176, v177 op_sel:[0,0,1]
	v_lshlrev_b32_e32 v185, 16, v185
	v_lshlrev_b32_e32 v184, 16, v181
	v_sub_f32_e32 v186, v177, v185
	v_pk_mul_f32 v[170:171], v[170:171], v[178:179] op_sel_hi:[1,0]
	v_sub_f32_e32 v184, v176, v184
	v_cvt_pk_bf16_f32 v186, v186, 0
	v_lshlrev_b32_e32 v174, 16, v183
	v_lshl_add_u64 v[176:177], v[202:203], 0, s[12:13]
	v_pk_fma_f32 v[170:171], v[10:11], v[170:171], v[18:19]
	v_cvt_pk_bf16_f32 v184, v184, 0
	v_and_or_b32 v181, v181, s35, v185
	v_and_or_b32 v174, v182, s35, v174
	v_lshlrev_b32_e32 v175, 16, v186
	global_store_dword v[176:177], v179, off
	v_add_u32_e32 v176, s48, v234
	v_pk_fma_f32 v[170:171], v[138:139], v[170:171], v[142:143]
	v_and_or_b32 v175, v184, s35, v175
	ds_write_b64 v176, v[180:181]
	ds_write_b64 v176, v[174:175] offset:33024
	v_pk_mul_f32 v[172:173], v[172:173], v[178:179] op_sel_hi:[1,0]
	v_cvt_pk_bf16_f32 v174, v170, 0
	v_pk_fma_f32 v[172:173], v[12:13], v[172:173], v[20:21]
	v_lshlrev_b32_e32 v175, 16, v174
	v_pk_fma_f32 v[172:173], v[140:141], v[172:173], v[144:145]
	v_sub_f32_e32 v175, v170, v175
	v_cvt_pk_bf16_f32 v176, v175, 0
	v_cvt_pk_bf16_f32 v175, v171, 0
	v_cvt_pk_bf16_f32 v181, v173, 0
	v_lshlrev_b32_e32 v175, 16, v175
	v_cvt_pk_bf16_f32 v179, v172, 0
	v_lshlrev_b32_e32 v181, 16, v181
	v_sub_f32_e32 v177, v171, v175
	v_lshlrev_b32_e32 v180, 16, v179
	v_and_or_b32 v174, v174, s35, v175
	v_and_or_b32 v175, v179, s35, v181
	v_mov_b32_e32 v179, v1
	v_cvt_pk_fp8_f32 v179, v170, v171
	s_add_u32 s12, s20, s12
	s_addc_u32 s13, s21, s13
	v_sub_f32_e32 v180, v172, v180
	v_cvt_pk_fp8_f32 v179, v172, v173 op_sel:[0,0,1]
	v_sub_f32_e32 v182, v173, v181
	v_lshl_add_u64 v[172:173], s[12:13], 0, v[0:1]
	v_cvt_pk_bf16_f32 v177, v177, 0
	v_pk_mul_f32 v[166:167], v[166:167], v[178:179] op_sel_hi:[1,0]
	global_store_dword v[172:173], v179, off
	v_pk_fma_f32 v[166:167], v[14:15], v[166:167], v[22:23]
	v_pk_mul_f32 v[168:169], v[168:169], v[178:179] op_sel_hi:[1,0]
	v_pk_fma_f32 v[166:167], v[150:151], v[166:167], v[146:147]
	v_mov_b32_e32 v179, v1
	v_cvt_pk_bf16_f32 v182, v182, 0
	v_lshlrev_b32_e32 v177, 16, v177
	v_cvt_pk_fp8_f32 v179, v166, v167
	v_cvt_pk_bf16_f32 v180, v180, 0
	v_and_or_b32 v170, v176, s35, v177
	v_lshlrev_b32_e32 v171, 16, v182
	v_add_u32_e32 v172, s48, v235
	v_and_or_b32 v171, v180, s35, v171
	ds_write_b64 v172, v[174:175]
	ds_write_b64 v172, v[170:171] offset:33024
	v_pk_fma_f32 v[168:169], v[16:17], v[168:169], v[24:25]
	v_cvt_pk_bf16_f32 v170, v166, 0
	v_pk_fma_f32 v[168:169], v[152:153], v[168:169], v[148:149]
	v_lshlrev_b32_e32 v171, 16, v170
	v_sub_f32_e32 v171, v166, v171
	v_cvt_pk_fp8_f32 v179, v168, v169 op_sel:[0,0,1]
	v_cvt_pk_bf16_f32 v172, v171, 0
	v_cvt_pk_bf16_f32 v171, v167, 0
	v_lshlrev_b32_e32 v171, 16, v171
	v_cvt_pk_bf16_f32 v176, v169, 0
	v_sub_f32_e32 v173, v167, v171
	v_cvt_pk_bf16_f32 v174, v168, 0
	v_lshlrev_b32_e32 v176, 16, v176
	v_cvt_pk_bf16_f32 v173, v173, 0
	v_lshlrev_b32_e32 v175, 16, v174
	v_sub_f32_e32 v177, v169, v176
	v_pk_mul_f32 v[162:163], v[162:163], v[178:179] op_sel_hi:[1,0]
	v_sub_f32_e32 v175, v168, v175
	v_cvt_pk_bf16_f32 v177, v177, 0
	v_lshlrev_b32_e32 v166, 16, v173
	v_lshl_add_u64 v[168:169], s[12:13], 0, v[198:199]
	v_pk_fma_f32 v[162:163], v[26:27], v[162:163], v[30:31]
	v_cvt_pk_bf16_f32 v175, v175, 0
	v_and_or_b32 v170, v170, s35, v171
	v_and_or_b32 v171, v174, s35, v176
	v_and_or_b32 v166, v172, s35, v166
	v_lshlrev_b32_e32 v167, 16, v177
	global_store_dword v[168:169], v179, off
	v_add_u32_e32 v168, s48, v236
	v_pk_fma_f32 v[162:163], v[154:155], v[162:163], v[158:159]
	v_mov_b32_e32 v174, v1
	v_and_or_b32 v167, v175, s35, v167
	ds_write_b64 v168, v[170:171]
	ds_write_b64 v168, v[166:167] offset:33024
	v_pk_mul_f32 v[164:165], v[164:165], v[178:179] op_sel_hi:[1,0]
	v_cvt_pk_bf16_f32 v166, v162, 0
	v_cvt_pk_fp8_f32 v174, v162, v163
	v_pk_fma_f32 v[164:165], v[28:29], v[164:165], v[32:33]
	v_lshlrev_b32_e32 v167, 16, v166
	v_pk_fma_f32 v[164:165], v[156:157], v[164:165], v[160:161]
	v_sub_f32_e32 v167, v162, v167
	v_cvt_pk_bf16_f32 v168, v167, 0
	v_cvt_pk_bf16_f32 v167, v163, 0
	v_cvt_pk_bf16_f32 v172, v165, 0
	v_lshlrev_b32_e32 v167, 16, v167
	v_cvt_pk_bf16_f32 v170, v164, 0
	v_lshlrev_b32_e32 v172, 16, v172
	v_cvt_pk_fp8_f32 v174, v164, v165 op_sel:[0,0,1]
	v_sub_f32_e32 v169, v163, v167
	v_lshlrev_b32_e32 v171, 16, v170
	v_sub_f32_e32 v173, v165, v172
	v_cvt_pk_bf16_f32 v169, v169, 0
	v_sub_f32_e32 v171, v164, v171
	v_cvt_pk_bf16_f32 v173, v173, 0
	v_cvt_pk_bf16_f32 v171, v171, 0
	v_lshlrev_b32_e32 v162, 16, v169
	v_lshlrev_b32_e32 v163, 16, v173
	v_lshl_add_u64 v[164:165], s[12:13], 0, v[200:201]
	v_and_or_b32 v166, v166, s35, v167
	v_and_or_b32 v167, v170, s35, v172
	v_and_or_b32 v162, v168, s35, v162
	v_and_or_b32 v163, v171, s35, v163
	global_store_dword v[164:165], v174, off
	v_add_u32_e32 v164, s48, v237
	ds_write_b64 v164, v[166:167]
	ds_write_b64 v164, v[162:163] offset:33024
	s_waitcnt lgkmcnt(0)
	s_barrier
	ds_read_b128 v[162:165], v238
	ds_read_b128 v[166:169], v238 offset:64
	s_waitcnt lgkmcnt(1)
	v_mfma_f32_16x16x32_bf16 v[170:173], v[162:165], v[34:37], 0
	ds_read_b128 v[174:177], v238 offset:33024
	ds_read_b128 v[178:181], v238 offset:33088
	s_mov_b64 s[34:35], -1
	s_mov_b64 s[12:13], -1
	v_mfma_f32_16x16x32_bf16 v[182:185], v[162:165], v[42:45], 0
	s_waitcnt lgkmcnt(1)
	v_mfma_f32_16x16x32_bf16 v[170:173], v[174:177], v[34:37], v[170:173]
	v_mfma_f32_16x16x32_bf16 v[174:177], v[174:177], v[42:45], v[182:185]
	v_mfma_f32_16x16x32_bf16 v[170:173], v[162:165], v[38:41], v[170:173]
	v_mfma_f32_16x16x32_bf16 v[162:165], v[162:165], v[46:49], v[174:177]
	v_mfma_f32_16x16x32_bf16 v[170:173], v[166:169], v[50:53], v[170:173]
	v_mfma_f32_16x16x32_bf16 v[162:165], v[166:169], v[58:61], v[162:165]
	s_waitcnt lgkmcnt(0)
	v_mfma_f32_16x16x32_bf16 v[170:173], v[178:181], v[50:53], v[170:173]
	v_mfma_f32_16x16x32_bf16 v[162:165], v[178:181], v[58:61], v[162:165]
	v_mfma_f32_16x16x32_bf16 v[170:173], v[166:169], v[54:57], v[170:173]
	v_mfma_f32_16x16x32_bf16 v[162:165], v[166:169], v[62:65], v[162:165]
	ds_read_b128 v[166:169], v238 offset:128
	ds_read_b128 v[174:177], v238 offset:192
	ds_read_b128 v[178:181], v238 offset:33152
	ds_read_b128 v[182:185], v238 offset:33216
	s_waitcnt lgkmcnt(3)
	v_mfma_f32_16x16x32_bf16 v[170:173], v[166:169], v[66:69], v[170:173]
	v_mfma_f32_16x16x32_bf16 v[162:165], v[166:169], v[74:77], v[162:165]
	s_waitcnt lgkmcnt(1)
	v_mfma_f32_16x16x32_bf16 v[170:173], v[178:181], v[66:69], v[170:173]
	v_mfma_f32_16x16x32_bf16 v[162:165], v[178:181], v[74:77], v[162:165]
	v_mfma_f32_16x16x32_bf16 v[170:173], v[166:169], v[70:73], v[170:173]
	v_mfma_f32_16x16x32_bf16 v[162:165], v[166:169], v[78:81], v[162:165]
	v_mfma_f32_16x16x32_bf16 v[166:169], v[174:177], v[82:85], v[170:173]
	v_mfma_f32_16x16x32_bf16 v[162:165], v[174:177], v[90:93], v[162:165]
	s_waitcnt lgkmcnt(0)
	v_mfma_f32_16x16x32_bf16 v[166:169], v[182:185], v[82:85], v[166:169]
	v_mfma_f32_16x16x32_bf16 v[162:165], v[182:185], v[90:93], v[162:165]
	v_mfma_f32_16x16x32_bf16 v[166:169], v[174:177], v[86:89], v[166:169]
	v_mfma_f32_16x16x32_bf16 v[162:165], v[174:177], v[94:97], v[162:165]
	s_nop 7
	ds_write2_b32 v239, v166, v162 offset1:16
	ds_write2_b32 v239, v167, v163 offset0:32 offset1:48
	ds_write2_b32 v239, v168, v164 offset0:64 offset1:80
	ds_write2_b32 v239, v169, v165 offset0:96 offset1:112
	s_waitcnt lgkmcnt(0)
	s_barrier
	ds_read2st64_b32 v[162:163], v233 offset1:8
	ds_read2st64_b32 v[164:165], v233 offset0:16 offset1:24
	s_waitcnt vmcnt(0) lgkmcnt(1)
	v_add_f32_e32 v162, v242, v162
	ds_read2st64_b32 v[166:167], v233 offset0:32 offset1:40
	v_add_f32_e32 v168, v162, v163
	ds_read2st64_b32 v[162:163], v233 offset0:48 offset1:56
	s_waitcnt lgkmcnt(2)
	v_add_f32_e32 v164, v168, v164
	v_add_f32_e32 v164, v164, v165
	s_waitcnt lgkmcnt(1)
	v_add_f32_e32 v164, v164, v166
	v_add_f32_e32 v164, v164, v167
	s_waitcnt lgkmcnt(0)
	v_add_f32_e32 v162, v164, v162
	v_add_f32_e32 v165, v162, v163
	ds_bpermute_b32 v162, v230, v165
	ds_bpermute_b32 v163, v230, v232
	s_waitcnt lgkmcnt(1)
	v_cmp_nlt_f32_e32 vcc, v165, v162
	s_and_saveexec_b64 s[36:37], vcc
	s_cbranch_execz .LBB0_988
	v_cmp_eq_f32_e32 vcc, v165, v162
	s_waitcnt lgkmcnt(0)
	v_cmp_lt_i32_e64 s[12:13], v163, v232
	s_and_b64 s[12:13], vcc, s[12:13]
	s_orn2_b64 s[12:13], s[12:13], exec

.LBB0_1402:
	s_waitcnt vmcnt(17)
	v_mov_b32_e32 v134, v123
	v_mov_b32_e32 v135, v124
	v_mov_b32_e32 v136, v122
	v_mov_b32_e32 v137, v125
	v_pk_add_f32 v[134:135], v[134:135], v[136:137]
	s_waitcnt vmcnt(16)
	v_mov_b32_e32 v136, v119
	v_mov_b32_e32 v137, v120
	v_mov_b32_e32 v190, v118
	v_mov_b32_e32 v191, v121
	v_pk_add_f32 v[136:137], v[136:137], v[190:191]
	v_add_f32_e32 v134, v134, v135
	v_pk_add_f32 v[136:137], v[136:137], v[136:137] op_sel:[0,1] op_sel_hi:[1,0]
	v_add_f32_e32 v134, 0, v134
	s_waitcnt vmcnt(7)
	v_add_f32_e32 v190, v130, v131
	v_add_f32_e32 v192, v132, v133
	s_waitcnt vmcnt(6)
	v_mov_b32_e32 v135, v126
	v_mov_b32_e32 v137, v127
	v_mov_b32_e32 v191, v128
	v_mov_b32_e32 v193, v129
	v_pk_add_f32 v[134:135], v[134:135], v[136:137]
	v_pk_add_f32 v[136:137], v[190:191], v[192:193]
	s_mov_b32 s4, 0xf800000
	v_pk_add_f32 v[134:135], v[134:135], v[136:137]
	s_add_u32 s6, s8, s24
	v_add_f32_e32 v134, v134, v135
	ds_bpermute_b32 v135, v206, v134
	s_addc_u32 s7, s9, s25
	s_add_i32 s14, s22, 0xffff0001
	s_waitcnt lgkmcnt(0)
	v_add_f32_e32 v134, v134, v135
	ds_bpermute_b32 v135, v207, v134
	s_waitcnt lgkmcnt(0)
	v_add_f32_e32 v134, v134, v135
	ds_bpermute_b32 v135, v208, v134
	s_waitcnt lgkmcnt(0)
	v_add_f32_e32 v134, v134, v135
	ds_bpermute_b32 v135, v209, v134
	s_waitcnt lgkmcnt(0)
	v_add_f32_e32 v134, v134, v135
	ds_bpermute_b32 v135, v224, v134
	s_waitcnt lgkmcnt(0)
	v_add_f32_e32 v134, v134, v135
	ds_bpermute_b32 v135, v225, v134
	s_waitcnt lgkmcnt(0)
	v_add_f32_e32 v194, v134, v135
	v_fmamk_f32 v123, v194, 0xba800000, v123
	v_fmamk_f32 v122, v194, 0xba800000, v122
	v_fmamk_f32 v125, v194, 0xba800000, v125
	v_fmac_f32_e32 v124, 0xba800000, v194
	v_pk_mul_f32 v[134:135], v[124:125], v[124:125]
	v_pk_mul_f32 v[136:137], v[122:123], v[122:123]
	v_fmamk_f32 v119, v194, 0xba800000, v119
	v_pk_mov_b32 v[190:191], v[136:137], v[134:135] op_sel:[1,0]
	v_mov_b32_e32 v137, v135
	v_fmamk_f32 v118, v194, 0xba800000, v118
	v_fmamk_f32 v121, v194, 0xba800000, v121
	v_pk_add_f32 v[134:135], v[190:191], v[136:137]
	v_fmac_f32_e32 v120, 0xba800000, v194
	v_pk_add_f32 v[134:135], v[134:135], v[134:135] op_sel_hi:[0,1]
	v_pk_mul_f32 v[136:137], v[120:121], v[120:121]
	v_pk_mul_f32 v[190:191], v[118:119], v[118:119]
	v_fmamk_f32 v130, v194, 0xba800000, v130
	v_pk_mov_b32 v[192:193], v[190:191], v[136:137] op_sel:[1,0]
	v_mov_b32_e32 v191, v137
	v_fmamk_f32 v131, v194, 0xba800000, v131
	v_fmac_f32_e32 v132, 0xba800000, v194
	v_mul_f32_e32 v134, v130, v130
	v_pk_add_f32 v[136:137], v[192:193], v[190:191]
	v_fmamk_f32 v133, v194, 0xba800000, v133
	v_pk_fma_f32 v[190:191], v[130:131], v[130:131], v[134:135] op_sel_hi:[1,1,0]
	v_mul_f32_e32 v134, v132, v132
	v_pk_add_f32 v[136:137], v[136:137], v[136:137] op_sel_hi:[0,1]
	v_pk_fma_f32 v[192:193], v[132:133], v[132:133], v[134:135] op_sel_hi:[1,1,0]
	v_fmamk_f32 v129, v194, 0xba800000, v129
	v_fmamk_f32 v128, v194, 0xba800000, v128
	v_fmamk_f32 v127, v194, 0xba800000, v127
	v_fmac_f32_e32 v126, 0xba800000, v194
	v_mul_f32_e32 v190, v126, v126
	v_mul_f32_e32 v192, v127, v127
	v_mul_f32_e32 v134, v128, v128
	v_mul_f32_e32 v136, v129, v129
	v_pk_add_f32 v[190:191], v[190:191], v[192:193]
	v_pk_add_f32 v[134:135], v[134:135], v[136:137]
	s_nop 0
	v_pk_add_f32 v[134:135], v[190:191], v[134:135]
	s_nop 0
	v_add_f32_e32 v134, v134, v135
	s_nop 1
	v_add_f32_dpp v134, v134, v134 quad_perm:[1,0,3,2] row_mask:0xf bank_mask:0xf
	s_nop 1
	v_add_f32_dpp v134, v134, v134 quad_perm:[2,3,0,1] row_mask:0xf bank_mask:0xf
	s_nop 1
	v_add_f32_dpp v134, v134, v134 row_half_mirror row_mask:0xf bank_mask:0xf
	s_nop 1
	v_add_f32_dpp v134, v134, v134 row_mirror row_mask:0xf bank_mask:0xf
	v_mov_b32_e32 v135, v134
	s_nop 1
	v_permlane16_swap_b32_e32 v135, v134
	s_nop 1
	v_add_f32_e32 v134, v134, v135
	v_mov_b32_e32 v135, v134
	s_nop 1
	v_permlane32_swap_b32_e32 v135, v134
	s_nop 1
	v_add_f32_e32 v134, v134, v135
	v_fmamk_f32 v134, v134, 0x3a800000, v211
	v_mul_f32_e32 v135, 0x4f800000, v134
	v_cmp_gt_f32_e32 vcc, s4, v134
	s_nop 1
	v_cndmask_b32_e32 v134, v134, v135, vcc
	v_sqrt_f32_e32 v135, v134
	s_nop 0
	v_add_u32_e32 v136, -1, v135
	v_add_u32_e32 v137, 1, v135
	v_fma_f32 v190, -v136, v135, v134
	v_fma_f32 v191, -v137, v135, v134
	v_cmp_ge_f32_e64 s[0:1], 0, v190
	s_nop 1
	v_cndmask_b32_e64 v135, v135, v136, s[0:1]
	v_cmp_lt_f32_e64 s[0:1], 0, v191
	s_nop 1
	v_cndmask_b32_e64 v135, v135, v137, s[0:1]
	v_mul_f32_e32 v136, 0x37800000, v135
	v_cndmask_b32_e32 v135, v135, v136, vcc
	v_cmp_class_f32_e32 vcc, v134, v212
	s_nop 1
	v_cndmask_b32_e32 v134, v135, v134, vcc
	v_div_scale_f32 v135, s[0:1], v134, v134, 1.0
	v_rcp_f32_e32 v136, v135
	s_mov_b32 s0, 0x3fb504f3
	v_fma_f32 v137, -v135, v136, 1.0
	v_fmac_f32_e32 v136, v137, v136
	v_div_scale_f32 v137, vcc, 1.0, v134, 1.0
	v_mul_f32_e32 v190, v137, v136
	v_fma_f32 v191, -v135, v190, v137
	v_fmac_f32_e32 v190, v191, v136
	v_fma_f32 v135, -v135, v190, v137
	v_div_fmas_f32 v135, v135, v136, v190
	v_div_fixup_f32 v134, v135, v134, 1.0
	v_pk_mul_f32 v[126:127], v[126:127], v[134:135] op_sel_hi:[1,0]
	v_pk_mul_f32 v[128:129], v[128:129], v[134:135] op_sel_hi:[1,0]
	v_pk_fma_f32 v[190:191], v[38:39], v[126:127], v[46:47]
	v_lshlrev_b32_e32 v126, 16, v182
	v_and_b32_e32 v127, 0xffff0000, v182
	v_pk_mul_f32 v[122:123], v[122:123], v[134:135] op_sel_hi:[1,0]
	v_pk_mul_f32 v[124:125], v[124:125], v[134:135] op_sel_hi:[1,0]
	v_pk_mul_f32 v[118:119], v[118:119], v[134:135] op_sel_hi:[1,0]
	v_pk_mul_f32 v[120:121], v[120:121], v[134:135] op_sel_hi:[1,0]
	v_pk_mul_f32 v[130:131], v[130:131], v[134:135] op_sel_hi:[1,0]
	v_pk_mul_f32 v[132:133], v[132:133], v[134:135] op_sel_hi:[1,0]
	v_pk_fma_f32 v[134:135], v[40:41], v[128:129], v[48:49]
	v_pk_fma_f32 v[126:127], v[114:115], v[126:127], 0 op_sel_hi:[0,1,0]
	v_lshlrev_b32_e32 v128, 16, v178
	v_and_b32_e32 v129, 0xffff0000, v178
	v_mov_b32_e32 v178, v115
	v_pk_fma_f32 v[126:127], v[178:179], v[128:129], v[126:127] op_sel_hi:[0,1,1]
	v_lshlrev_b32_e32 v128, 16, v176
	v_and_b32_e32 v129, 0xffff0000, v176
	v_pk_fma_f32 v[126:127], v[116:117], v[128:129], v[126:127] op_sel_hi:[0,1,1]
	v_lshlrev_b32_e32 v128, 16, v174
	v_and_b32_e32 v129, 0xffff0000, v174
	v_mov_b32_e32 v174, v117
	v_pk_fma_f32 v[128:129], v[174:175], v[128:129], v[126:127] op_sel_hi:[0,1,1]
	v_lshlrev_b32_e32 v126, 16, v183
	v_and_b32_e32 v127, 0xffff0000, v183
	v_pk_fma_f32 v[136:137], v[36:37], v[132:133], v[44:45]
	v_pk_fma_f32 v[126:127], v[114:115], v[126:127], 0 op_sel_hi:[0,1,0]
	v_lshlrev_b32_e32 v132, 16, v179
	v_and_b32_e32 v133, 0xffff0000, v179
	v_pk_fma_f32 v[126:127], v[178:179], v[132:133], v[126:127] op_sel_hi:[0,1,1]
	v_lshlrev_b32_e32 v132, 16, v177
	v_and_b32_e32 v133, 0xffff0000, v177
	v_pk_fma_f32 v[124:125], v[4:5], v[124:125], v[12:13]
	v_pk_fma_f32 v[122:123], v[2:3], v[122:123], v[10:11]
	v_pk_fma_f32 v[126:127], v[116:117], v[132:133], v[126:127] op_sel_hi:[0,1,1]
	v_lshlrev_b32_e32 v132, 16, v175
	v_and_b32_e32 v133, 0xffff0000, v175
	v_pk_fma_f32 v[126:127], v[174:175], v[132:133], v[126:127] op_sel_hi:[0,1,1]
	v_pk_mul_f32 v[122:123], v[122:123], s[0:1] op_sel_hi:[1,0]
	v_pk_mul_f32 v[124:125], v[124:125], s[0:1] op_sel_hi:[1,0]
	v_pk_fma_f32 v[128:129], v[66:67], v[128:129], v[122:123]
	v_pk_fma_f32 v[126:127], v[68:69], v[126:127], v[124:125]
	v_mov_b32_e32 v124, v128
	v_pk_mov_b32 v[122:123], v[128:129], v[126:127] op_sel:[1,0]
	v_mov_b32_e32 v125, v127
	v_pk_add_f32 v[122:123], v[122:123], v[124:125]
	v_lshlrev_b32_e32 v124, 16, v168
	v_add_f32_e32 v115, v122, v123
	v_add_f32_e32 v115, 0, v115
	v_lshlrev_b32_e32 v122, 16, v172
	v_and_b32_e32 v123, 0xffff0000, v172
	v_pk_fma_f32 v[122:123], v[114:115], v[122:123], 0 op_sel_hi:[0,1,0]
	v_and_b32_e32 v125, 0xffff0000, v168
	v_pk_fma_f32 v[122:123], v[178:179], v[124:125], v[122:123] op_sel_hi:[0,1,1]
	v_lshlrev_b32_e32 v124, 16, v164
	v_and_b32_e32 v125, 0xffff0000, v164
	v_pk_fma_f32 v[122:123], v[116:117], v[124:125], v[122:123] op_sel_hi:[0,1,1]
	v_lshlrev_b32_e32 v124, 16, v160
	v_and_b32_e32 v125, 0xffff0000, v160
	v_pk_fma_f32 v[122:123], v[174:175], v[124:125], v[122:123] op_sel_hi:[0,1,1]
	v_lshlrev_b32_e32 v124, 16, v173
	v_and_b32_e32 v125, 0xffff0000, v173
	v_pk_fma_f32 v[124:125], v[114:115], v[124:125], 0 op_sel_hi:[0,1,0]
	v_lshlrev_b32_e32 v132, 16, v169
	v_and_b32_e32 v133, 0xffff0000, v169
	v_pk_fma_f32 v[124:125], v[178:179], v[132:133], v[124:125] op_sel_hi:[0,1,1]
	v_lshlrev_b32_e32 v132, 16, v165
	v_and_b32_e32 v133, 0xffff0000, v165
	v_pk_fma_f32 v[120:121], v[8:9], v[120:121], v[16:17]
	v_pk_fma_f32 v[118:119], v[6:7], v[118:119], v[14:15]
	v_pk_fma_f32 v[124:125], v[116:117], v[132:133], v[124:125] op_sel_hi:[0,1,1]
	v_lshlrev_b32_e32 v132, 16, v161
	v_and_b32_e32 v133, 0xffff0000, v161
	v_pk_fma_f32 v[124:125], v[174:175], v[132:133], v[124:125] op_sel_hi:[0,1,1]
	v_pk_mul_f32 v[118:119], v[118:119], s[0:1] op_sel_hi:[1,0]
	v_pk_mul_f32 v[120:121], v[120:121], s[0:1] op_sel_hi:[1,0]
	v_pk_fma_f32 v[132:133], v[78:79], v[122:123], v[118:119]
	v_pk_fma_f32 v[120:121], v[80:81], v[124:125], v[120:121]
	v_mov_b32_e32 v122, v132
	v_pk_mov_b32 v[118:119], v[132:133], v[120:121] op_sel:[1,0]
	v_mov_b32_e32 v123, v121
	v_pk_add_f32 v[118:119], v[118:119], v[122:123]
	v_lshlrev_b32_e32 v122, 16, v186
	v_pk_add_f32 v[160:161], v[118:119], v[118:119] op_sel_hi:[0,1]
	v_lshlrev_b32_e32 v118, 16, v188
	v_and_b32_e32 v119, 0xffff0000, v188
	v_pk_fma_f32 v[118:119], v[114:115], v[118:119], 0 op_sel_hi:[0,1,0]
	v_and_b32_e32 v123, 0xffff0000, v186
	v_pk_fma_f32 v[118:119], v[178:179], v[122:123], v[118:119] op_sel_hi:[0,1,1]
	v_lshlrev_b32_e32 v122, 16, v184
	v_and_b32_e32 v123, 0xffff0000, v184
	v_pk_fma_f32 v[118:119], v[116:117], v[122:123], v[118:119] op_sel_hi:[0,1,1]
	v_lshlrev_b32_e32 v122, 16, v180
	v_and_b32_e32 v123, 0xffff0000, v180
	v_pk_fma_f32 v[118:119], v[174:175], v[122:123], v[118:119] op_sel_hi:[0,1,1]
	v_lshlrev_b32_e32 v122, 16, v189
	v_and_b32_e32 v123, 0xffff0000, v189
	v_pk_fma_f32 v[122:123], v[114:115], v[122:123], 0 op_sel_hi:[0,1,0]
	v_lshlrev_b32_e32 v124, 16, v187
	v_and_b32_e32 v125, 0xffff0000, v187
	v_pk_fma_f32 v[122:123], v[178:179], v[124:125], v[122:123] op_sel_hi:[0,1,1]
	v_lshlrev_b32_e32 v124, 16, v185
	v_and_b32_e32 v125, 0xffff0000, v185
	v_pk_fma_f32 v[130:131], v[34:35], v[130:131], v[42:43]
	v_pk_fma_f32 v[122:123], v[116:117], v[124:125], v[122:123] op_sel_hi:[0,1,1]
	v_lshlrev_b32_e32 v124, 16, v181
	v_and_b32_e32 v125, 0xffff0000, v181
	v_pk_fma_f32 v[122:123], v[174:175], v[124:125], v[122:123] op_sel_hi:[0,1,1]
	v_pk_mul_f32 v[124:125], v[130:131], s[0:1] op_sel_hi:[1,0]
	v_pk_mul_f32 v[130:131], v[136:137], s[0:1] op_sel_hi:[1,0]
	v_pk_fma_f32 v[124:125], v[98:99], v[118:119], v[124:125]
	s_waitcnt vmcnt(5)
	v_lshlrev_b32_e32 v118, 16, v170
	v_and_b32_e32 v119, 0xffff0000, v170
	v_pk_fma_f32 v[122:123], v[100:101], v[122:123], v[130:131]
	v_pk_fma_f32 v[118:119], v[114:115], v[118:119], 0 op_sel_hi:[0,1,0]
	s_waitcnt vmcnt(4)
	v_lshlrev_b32_e32 v130, 16, v166
	v_and_b32_e32 v131, 0xffff0000, v166
	v_add_f32_e32 v117, v124, v125
	v_pk_fma_f32 v[118:119], v[178:179], v[130:131], v[118:119] op_sel_hi:[0,1,1]
	s_waitcnt vmcnt(3)
	v_lshlrev_b32_e32 v130, 16, v162
	v_and_b32_e32 v131, 0xffff0000, v162
	v_pk_fma_f32 v[118:119], v[116:117], v[130:131], v[118:119] op_sel_hi:[0,1,1]
	s_waitcnt vmcnt(2)
	v_lshlrev_b32_e32 v130, 16, v158
	v_and_b32_e32 v131, 0xffff0000, v158
	v_pk_fma_f32 v[130:131], v[174:175], v[130:131], v[118:119] op_sel_hi:[0,1,1]
	v_lshlrev_b32_e32 v118, 16, v171
	v_and_b32_e32 v119, 0xffff0000, v171
	v_pk_fma_f32 v[118:119], v[114:115], v[118:119], 0 op_sel_hi:[0,1,0]
	v_lshlrev_b32_e32 v164, 16, v167
	v_and_b32_e32 v165, 0xffff0000, v167
	v_pk_fma_f32 v[118:119], v[178:179], v[164:165], v[118:119] op_sel_hi:[0,1,1]
	v_lshlrev_b32_e32 v162, 16, v163
	v_and_b32_e32 v163, 0xffff0000, v163
	v_pk_fma_f32 v[118:119], v[116:117], v[162:163], v[118:119] op_sel_hi:[0,1,1]
	v_lshlrev_b32_e32 v158, 16, v159
	v_and_b32_e32 v159, 0xffff0000, v159
	v_pk_fma_f32 v[118:119], v[174:175], v[158:159], v[118:119] op_sel_hi:[0,1,1]
	v_pk_mul_f32 v[158:159], v[190:191], s[0:1] op_sel_hi:[1,0]
	v_pk_mul_f32 v[134:135], v[134:135], s[0:1] op_sel_hi:[1,0]
	v_pk_fma_f32 v[130:131], v[102:103], v[130:131], v[158:159]
	v_pk_fma_f32 v[118:119], v[104:105], v[118:119], v[134:135]
	v_add_f32_e32 v137, v122, v123
	v_mov_b32_e32 v116, v130
	v_mov_b32_e32 v136, v131
	v_mov_b32_e32 v160, v118
	v_mov_b32_e32 v114, v119
	v_pk_add_f32 v[116:117], v[116:117], v[136:137]
	v_pk_add_f32 v[114:115], v[160:161], v[114:115]
	s_nop 0
	v_pk_add_f32 v[114:115], v[116:117], v[114:115]
	s_nop 0
	v_add_f32_e32 v114, v114, v115
	ds_bpermute_b32 v115, v206, v114
	s_waitcnt lgkmcnt(0)
	v_add_f32_e32 v114, v114, v115
	ds_bpermute_b32 v115, v207, v114
	s_waitcnt lgkmcnt(0)
	v_add_f32_e32 v114, v114, v115
	ds_bpermute_b32 v115, v208, v114
	s_waitcnt lgkmcnt(0)
	v_add_f32_e32 v114, v114, v115
	ds_bpermute_b32 v115, v209, v114
	s_waitcnt lgkmcnt(0)
	v_add_f32_e32 v114, v114, v115
	ds_bpermute_b32 v115, v224, v114
	s_waitcnt lgkmcnt(0)
	v_add_f32_e32 v114, v114, v115
	ds_bpermute_b32 v115, v225, v114
	s_waitcnt lgkmcnt(0)
	v_add_f32_e32 v158, v114, v115
	v_fmamk_f32 v129, v158, 0xba800000, v129
	v_fmac_f32_e32 v128, 0xba800000, v158
	v_fmamk_f32 v127, v158, 0xba800000, v127
	v_fmac_f32_e32 v126, 0xba800000, v158
	v_pk_mul_f32 v[114:115], v[126:127], v[126:127]
	v_pk_mul_f32 v[116:117], v[128:129], v[128:129]
	v_fmamk_f32 v121, v158, 0xba800000, v121
	v_pk_mov_b32 v[134:135], v[116:117], v[114:115] op_sel:[1,0]
	v_mov_b32_e32 v117, v115
	v_pk_add_f32 v[114:115], v[134:135], v[116:117]
	v_fmac_f32_e32 v120, 0xba800000, v158
	v_fmamk_f32 v133, v158, 0xba800000, v133
	v_fmac_f32_e32 v132, 0xba800000, v158
	v_pk_add_f32 v[114:115], v[114:115], v[114:115] op_sel_hi:[0,1]
	v_pk_mul_f32 v[116:117], v[120:121], v[120:121]
	v_pk_mul_f32 v[134:135], v[132:133], v[132:133]
	v_fmac_f32_e32 v124, 0xba800000, v158
	v_pk_mov_b32 v[136:137], v[134:135], v[116:117] op_sel:[1,0]
	v_mov_b32_e32 v135, v117
	v_fmac_f32_e32 v122, 0xba800000, v158
	v_fmamk_f32 v125, v158, 0xba800000, v125
	v_mul_f32_e32 v114, v124, v124
	v_pk_add_f32 v[116:117], v[136:137], v[134:135]
	v_fmamk_f32 v123, v158, 0xba800000, v123
	v_pk_fma_f32 v[134:135], v[124:125], v[124:125], v[114:115] op_sel_hi:[1,1,0]
	v_mul_f32_e32 v114, v122, v122
	v_pk_add_f32 v[116:117], v[116:117], v[116:117] op_sel_hi:[0,1]
	v_pk_fma_f32 v[136:137], v[122:123], v[122:123], v[114:115] op_sel_hi:[1,1,0]
	v_fmamk_f32 v119, v158, 0xba800000, v119
	v_fmac_f32_e32 v118, 0xba800000, v158
	v_fmamk_f32 v131, v158, 0xba800000, v131
	v_fmac_f32_e32 v130, 0xba800000, v158
	v_mul_f32_e32 v134, v130, v130
	v_mul_f32_e32 v136, v131, v131
	v_mul_f32_e32 v114, v118, v118
	v_mul_f32_e32 v116, v119, v119
	v_pk_add_f32 v[134:135], v[134:135], v[136:137]
	v_pk_add_f32 v[114:115], v[114:115], v[116:117]
	s_nop 0
	v_pk_add_f32 v[114:115], v[134:135], v[114:115]
	s_nop 0
	v_add_f32_e32 v114, v114, v115
	s_nop 1
	v_add_f32_dpp v114, v114, v114 quad_perm:[1,0,3,2] row_mask:0xf bank_mask:0xf
	s_nop 1
	v_add_f32_dpp v114, v114, v114 quad_perm:[2,3,0,1] row_mask:0xf bank_mask:0xf
	s_nop 1
	v_add_f32_dpp v114, v114, v114 row_half_mirror row_mask:0xf bank_mask:0xf
	s_nop 1
	v_add_f32_dpp v114, v114, v114 row_mirror row_mask:0xf bank_mask:0xf
	v_mov_b32_e32 v115, v114
	s_nop 1
	v_permlane16_swap_b32_e32 v115, v114
	s_nop 1
	v_add_f32_e32 v114, v114, v115
	v_mov_b32_e32 v115, v114
	s_nop 1
	v_permlane32_swap_b32_e32 v115, v114
	s_nop 1
	v_add_f32_e32 v114, v114, v115
	v_fmamk_f32 v114, v114, 0x3a800000, v211
	v_mul_f32_e32 v115, 0x4f800000, v114
	v_cmp_gt_f32_e32 vcc, s4, v114
	s_lshl_b64 s[4:5], s[14:15], 12
	s_nop 0
	v_cndmask_b32_e32 v114, v114, v115, vcc
	v_sqrt_f32_e32 v115, v114
	s_nop 0
	v_add_u32_e32 v116, -1, v115
	v_fma_f32 v117, -v116, v115, v114
	v_cmp_ge_f32_e64 s[0:1], 0, v117
	v_add_u32_e32 v117, 1, v115
	s_nop 0
	v_cndmask_b32_e64 v116, v115, v116, s[0:1]
	v_fma_f32 v115, -v117, v115, v114
	v_cmp_lt_f32_e64 s[0:1], 0, v115
	s_nop 1
	v_cndmask_b32_e64 v115, v116, v117, s[0:1]
	v_mul_f32_e32 v116, 0x37800000, v115
	v_cndmask_b32_e32 v115, v115, v116, vcc
	v_cmp_class_f32_e32 vcc, v114, v212
	s_nop 1
	v_cndmask_b32_e32 v114, v115, v114, vcc
	v_div_scale_f32 v115, s[0:1], v114, v114, 1.0
	v_rcp_f32_e32 v116, v115
	s_add_u32 s0, s36, s4
	s_addc_u32 s1, s37, s5
	s_cmp_lt_i32 s10, 0x10000
	v_fma_f32 v117, -v115, v116, 1.0
	v_fmac_f32_e32 v116, v117, v116
	v_div_scale_f32 v117, vcc, 1.0, v114, 1.0
	v_mul_f32_e32 v134, v117, v116
	v_fma_f32 v135, -v115, v134, v117
	v_fmac_f32_e32 v134, v135, v116
	v_fma_f32 v115, -v115, v134, v117
	v_div_fmas_f32 v115, v115, v116, v134
	v_div_fixup_f32 v134, v115, v114, 1.0
	v_mov_b32_e32 v135, v134
	v_pk_mul_f32 v[114:115], v[128:129], v[134:135] op_sel_hi:[1,0]
	v_pk_mul_f32 v[116:117], v[126:127], v[134:135] op_sel_hi:[1,0]
	s_cselect_b32 s1, s7, s1
	s_cselect_b32 s0, s6, s0
	v_pk_fma_f32 v[116:117], v[20:21], v[116:117], v[28:29]
	v_pk_fma_f32 v[114:115], v[18:19], v[114:115], v[26:27]
	v_lshl_add_u64 v[126:127], s[0:1], 0, v[0:1]
	global_store_dwordx4 v0, v[114:117], s[0:1]
	s_mov_b64 s[0:1], -1
	s_and_b64 vcc, exec, s[2:3]
	v_pk_mul_f32 v[128:129], v[132:133], v[134:135]
	s_cbranch_vccz .LBB0_1404
	v_mov_b32_e32 v132, v134
	v_mov_b32_e32 v133, v134
	v_pk_mul_f32 v[132:133], v[120:121], v[132:133]
	v_pk_fma_f32 v[158:159], v[22:23], v[128:129], v[30:31]
	v_pk_fma_f32 v[160:161], v[24:25], v[132:133], v[32:33]
	global_store_dwordx4 v[126:127], v[158:161], off offset:1024
	s_mov_b64 s[0:1], 0
